# attention cross-half max/sum exchange via v_permlane32_swap instead of ds_bpermute round trips (MLA and stick-breaking loops)
# speedup vs baseline: 1.0004x; 1.0004x over previous
; template <bool MLA>
; __device__ __forceinline__ void attn_unit(const P& p, LAS unsigned char* lds, const int b, const int h, const int qb) {
;     ...
;                 for (int r = 0; r < 16; ++r) pm = fmaxf(pm, fmaxf(p0[r], p1[r]));
;                 pm = fmaxf(pm, __shfl_xor(pm, 32));
;                 const float mn = fmaxf(m_run, pm), alpha = __builtin_amdgcn_exp2f(m_run - mn); m_run = mn;
;                 float ps = 0.f;
; #pragma unroll
;                 for (int r = 0; r < 16; ++r) { p0[r] = __builtin_amdgcn_exp2f(p0[r] - mn); p1[r] = __builtin_amdgcn_exp2f(p1[r] - mn); ps += p0[r] + p1[r]; }
;                 ps += __shfl_xor(ps, 32);
;                 l_run = l_run * alpha + ps;
;                 if (__any(alpha < 1.f)) { if (hi == 0) al[r32] = alpha; asm volatile("s_waitcnt lgkmcnt(0)" ::: "memory");
; #pragma unroll
;                     for (int r = 0; r < 16; ++r) { const float a = al[(r & 3) + 8 * (r >> 2) + 4 * hi];
; #pragma unroll
;                         for (int d0 = 0; d0 < 4; ++d0) o[d0][r] *= a; } }
.LBB0_711:
	s_nop 8
	s_mov_b32 s0, 0xff61b1e6
	v_max3_f32 v3, v82, v83, s0
	v_max3_f32 v4, v84, v85, v86
	v_max3_f32 v5, v87, v88, v89
	v_max3_f32 v3, v3, v90, v91
	v_max3_f32 v4, v4, v92, v93
	v_max3_f32 v5, v5, v94, v95
	v_max3_f32 v3, v3, v96, v97
	v_max3_f32 v4, v4, v98, v99
	v_max3_f32 v5, v5, v100, v101
	v_max3_f32 v3, v3, v102, v103
	v_max3_f32 v4, v4, v104, v105
	v_max3_f32 v5, v5, v106, v107
	v_max3_f32 v3, v3, v108, v109
	v_max3_f32 v4, v4, v110, v111
	v_max3_f32 v5, v5, v112, v113
	v_max3_f32 v3, v3, v4, v5
	v_mov_b32_e32 v4, v3
	s_nop 1
	v_permlane32_swap_b32 v3, v4
	v_max_f32_e32 v3, v3, v4
	v_add_f32_e32 v4, 0xc1000000, v3
	v_cmp_gt_f32_e32 vcc, v4, v216
	s_nop 1
	v_cndmask_b32_e32 v3, v216, v3, vcc
	v_sub_f32_e32 v4, v82, v3
	v_exp_f32_e32 v10, v4
	v_sub_f32_e32 v4, v98, v3
	v_exp_f32_e32 v4, v4
	v_sub_f32_e32 v5, v83, v3
	v_exp_f32_e32 v12, v5
	v_sub_f32_e32 v5, v99, v3
	v_add_f32_e32 v6, v10, v4
	v_add_f32_e32 v8, 0, v6
	v_sub_f32_e32 v6, v84, v3
	v_exp_f32_e32 v5, v5
	v_exp_f32_e32 v14, v6
	v_sub_f32_e32 v6, v100, v3
	v_exp_f32_e32 v6, v6
	v_add_f32_e32 v9, v12, v5
	v_sub_f32_e32 v7, v85, v3
	v_add_f32_e32 v8, v9, v8
	v_add_f32_e32 v9, v14, v6
	v_exp_f32_e32 v16, v7
	v_sub_f32_e32 v7, v101, v3
	v_add_f32_e32 v11, v9, v8
	v_sub_f32_e32 v8, v86, v3
	v_exp_f32_e32 v7, v7
	v_exp_f32_e32 v84, v8
	v_sub_f32_e32 v8, v102, v3
	v_exp_f32_e32 v8, v8
	v_add_f32_e32 v13, v16, v7
	v_sub_f32_e32 v9, v87, v3
	v_add_f32_e32 v11, v13, v11
	v_add_f32_e32 v13, v84, v8
	v_exp_f32_e32 v87, v9
	v_sub_f32_e32 v9, v103, v3
	v_add_f32_e32 v15, v13, v11
	v_sub_f32_e32 v11, v88, v3
	v_exp_f32_e32 v9, v9
	v_exp_f32_e32 v98, v11
	v_sub_f32_e32 v11, v104, v3
	v_exp_f32_e32 v11, v11
	v_add_f32_e32 v17, v87, v9
	v_sub_f32_e32 v13, v89, v3
	v_add_f32_e32 v15, v17, v15
	v_add_f32_e32 v17, v98, v11
	v_exp_f32_e32 v99, v13
	v_sub_f32_e32 v13, v105, v3
	v_add_f32_e32 v82, v17, v15
	v_sub_f32_e32 v15, v90, v3
	v_exp_f32_e32 v13, v13
	v_exp_f32_e32 v83, v15
	v_sub_f32_e32 v15, v106, v3
	v_exp_f32_e32 v15, v15
	v_add_f32_e32 v85, v99, v13
	v_sub_f32_e32 v17, v91, v3
	v_add_f32_e32 v82, v85, v82
	v_add_f32_e32 v85, v83, v15
	v_exp_f32_e32 v86, v17
	v_sub_f32_e32 v17, v107, v3
	v_add_f32_e32 v89, v85, v82
	v_sub_f32_e32 v82, v92, v3
	v_exp_f32_e32 v17, v17
	v_exp_f32_e32 v88, v82
	v_sub_f32_e32 v82, v108, v3
	v_exp_f32_e32 v82, v82
	v_add_f32_e32 v91, v86, v17
	v_sub_f32_e32 v85, v93, v3
	v_add_f32_e32 v89, v91, v89
	v_add_f32_e32 v91, v88, v82
	v_exp_f32_e32 v90, v85
	v_sub_f32_e32 v85, v109, v3
	v_add_f32_e32 v93, v91, v89
	v_sub_f32_e32 v89, v94, v3
	v_exp_f32_e32 v85, v85
	v_exp_f32_e32 v92, v89
	v_sub_f32_e32 v89, v110, v3
	v_exp_f32_e32 v89, v89
	v_add_f32_e32 v100, v90, v85
	v_sub_f32_e32 v91, v95, v3
	v_add_f32_e32 v93, v100, v93
	v_add_f32_e32 v95, v92, v89
	v_exp_f32_e32 v94, v91
	v_sub_f32_e32 v91, v111, v3
	v_add_f32_e32 v100, v95, v93
	v_sub_f32_e32 v93, v96, v3
	v_exp_f32_e32 v91, v91
	v_exp_f32_e32 v101, v93
	v_sub_f32_e32 v93, v112, v3
	v_sub_f32_e32 v95, v97, v3
	v_exp_f32_e32 v93, v93
	v_exp_f32_e32 v102, v95
	v_sub_f32_e32 v95, v113, v3
	v_exp_f32_e32 v95, v95
	v_add_f32_e32 v103, v94, v91
	v_add_f32_e32 v96, v103, v100
	v_add_f32_e32 v97, v101, v93
	v_add_f32_e32 v97, v97, v96
	v_add_f32_e32 v100, v102, v95
	v_sub_f32_e32 v216, v216, v3
	v_add_f32_e32 v97, v100, v97
	v_exp_f32_e32 v96, v216
	v_mov_b32_e32 v100, v97
	s_nop 1
	v_permlane32_swap_b32 v97, v100
	v_cmp_gt_f32_e32 vcc, 1.0, v96
	s_cbranch_vccz .LBB0_715
	s_and_saveexec_b64 s[0:1], s[4:5]
	ds_write_b32 v212, v96
	s_or_b64 exec, exec, s[0:1]
	s_waitcnt lgkmcnt(0)
	ds_read_b128 v[104:107], v214 offset:96
	ds_read_b128 v[108:111], v214 offset:64
	ds_read_b128 v[216:219], v214 offset:32
	ds_read_b128 v[220:223], v214
	s_waitcnt lgkmcnt(3)
	v_pk_mul_f32 v[80:81], v[80:81], v[106:107]
	s_waitcnt lgkmcnt(2)
	v_pk_mul_f32 v[76:77], v[76:77], v[110:111]
	s_waitcnt lgkmcnt(1)
	v_pk_mul_f32 v[72:73], v[72:73], v[218:219]
	s_waitcnt lgkmcnt(0)
	v_pk_mul_f32 v[68:69], v[68:69], v[222:223]
	v_pk_mul_f32 v[78:79], v[78:79], v[104:105]
	v_pk_mul_f32 v[74:75], v[74:75], v[108:109]
	v_pk_mul_f32 v[70:71], v[70:71], v[216:217]
	v_pk_mul_f32 v[66:67], v[66:67], v[220:221]
	v_pk_mul_f32 v[64:65], v[64:65], v[106:107]
	v_pk_mul_f32 v[60:61], v[60:61], v[110:111]
	v_pk_mul_f32 v[56:57], v[56:57], v[218:219]
	v_pk_mul_f32 v[52:53], v[52:53], v[222:223]
	v_pk_mul_f32 v[62:63], v[62:63], v[104:105]
	v_pk_mul_f32 v[58:59], v[58:59], v[108:109]
	v_pk_mul_f32 v[54:55], v[54:55], v[216:217]
	v_pk_mul_f32 v[50:51], v[50:51], v[220:221]
	v_pk_mul_f32 v[48:49], v[48:49], v[106:107]
	v_pk_mul_f32 v[44:45], v[44:45], v[110:111]
	v_pk_mul_f32 v[40:41], v[40:41], v[218:219]
	v_pk_mul_f32 v[36:37], v[36:37], v[222:223]
	v_pk_mul_f32 v[46:47], v[46:47], v[104:105]
	v_pk_mul_f32 v[42:43], v[42:43], v[108:109]
	v_pk_mul_f32 v[38:39], v[38:39], v[216:217]
	v_pk_mul_f32 v[34:35], v[34:35], v[220:221]
	v_pk_mul_f32 v[32:33], v[32:33], v[106:107]
	v_pk_mul_f32 v[28:29], v[28:29], v[110:111]
	v_pk_mul_f32 v[24:25], v[24:25], v[218:219]
	v_pk_mul_f32 v[20:21], v[20:21], v[222:223]
	v_pk_mul_f32 v[30:31], v[30:31], v[104:105]
	v_pk_mul_f32 v[26:27], v[26:27], v[108:109]
	v_pk_mul_f32 v[22:23], v[22:23], v[216:217]
	v_pk_mul_f32 v[18:19], v[18:19], v[220:221]

; __device__ __forceinline__ unsigned pk2(float a, float b) { f32x2_t v = {a, b}; bf16x2_t r = __builtin_convertvector(v, bf16x2_t); return __builtin_bit_cast(unsigned, r); }
; template <bool MLA>
; __device__ __forceinline__ void attn_unit(const P& p, LAS unsigned char* lds, const int b, const int h, const int qb) {
;     ...
;                 float lsum = 0.f; bf16x8 lf[4];
; #pragma unroll
;                 for (int g = 0; g < 4; ++g) {
;                     float Lv[8];
; #pragma unroll
;                     for (int j = 0; j < 8; ++j) { const int r = 8 * (g & 1) + j;
;                         const float z = (g < 2 ? p0[r] : p1[r]);
;                         const float t = __builtin_amdgcn_logf(1.f + __builtin_amdgcn_exp2f(-fabsf(z)));
;                         const float L = -(fmaxf(z, 0.f) + t);
;                         const float ls = fminf(z, 0.f) - t;
;                         if (g < 2) p0[r] = ls; else p1[r] = ls;
;                         Lv[j] = L; lsum += L; }
;                     u32x4 w; w.x = pk2(Lv[0], Lv[1]); w.y = pk2(Lv[2], Lv[3]); w.z = pk2(Lv[4], Lv[5]); w.w = pk2(Lv[6], Lv[7]); lf[g] = __builtin_bit_cast(bf16x8, w);
;                 }
.LBB0_748:
	s_nop 7
	v_exp_f32_e64 v3, -|v98|
	v_exp_f32_e64 v6, -|v99|
	v_exp_f32_e64 v7, -|v101|
	v_max_f32_e32 v13, v100, v100
	v_add_f32_e32 v3, 1.0, v3
	v_log_f32_e32 v8, v3
	v_add_f32_e32 v3, 1.0, v6
	v_exp_f32_e64 v6, -|v100|
	v_log_f32_e32 v9, v3
	v_max_f32_e32 v3, v99, v99
	v_exp_f32_e64 v16, -|v102|
	v_exp_f32_e64 v17, -|v103|
	v_max_f32_e32 v99, v102, v102
	v_max_f32_e32 v100, v103, v103
	v_max_f32_e32 v5, v98, v98
	v_max_f32_e32 v15, v101, v101
	v_max_f32_e32 v98, 0, v99
	v_min_f32_e32 v102, 0, v99
	v_max_f32_e32 v99, 0, v100
	v_min_f32_e32 v103, 0, v100
	v_exp_f32_e64 v100, -|v104|
	v_exp_f32_e64 v101, -|v105|
	v_add_f32_e32 v6, 1.0, v6
	v_add_f32_e32 v7, 1.0, v7
	v_log_f32_e32 v12, v6
	v_max_f32_e32 v6, 0, v13
	v_min_f32_e32 v14, 0, v13
	v_log_f32_e32 v13, v7
	v_add_f32_e32 v16, 1.0, v16
	v_add_f32_e32 v17, 1.0, v17
	v_max_f32_e32 v4, 0, v5
	v_min_f32_e32 v10, 0, v5
	v_max_f32_e32 v5, 0, v3
	v_log_f32_e32 v16, v16
	v_log_f32_e32 v17, v17
	v_add_f32_e32 v100, 1.0, v100
	v_add_f32_e32 v101, 1.0, v101
	v_pk_add_f32 v[4:5], v[4:5], v[8:9]
	v_max_f32_e32 v7, 0, v15
	v_log_f32_e32 v192, v100
	v_log_f32_e32 v193, v101
	v_min_f32_e32 v11, 0, v3
	v_sub_f32_e64 v3, -v4, v5
	v_pk_add_f32 v[6:7], v[6:7], v[12:13]
	v_max_f32_e32 v104, v104, v104
	v_sub_f32_e32 v3, v3, v6
	v_max_f32_e32 v105, v105, v105
	v_sub_f32_e32 v3, v3, v7
	v_pk_add_f32 v[98:99], v[98:99], v[16:17]
	v_max_f32_e32 v100, 0, v104
	v_max_f32_e32 v101, 0, v105
	v_sub_f32_e32 v3, v3, v98
	v_pk_add_f32 v[100:101], v[100:101], v[192:193]
	v_pk_add_f32 v[4:5], v[4:5], 0 neg_lo:[1,1] neg_hi:[1,1]
	v_pk_add_f32 v[6:7], v[6:7], 0 neg_lo:[1,1] neg_hi:[1,1]
	v_sub_f32_e32 v3, v3, v99
	v_cvt_pk_bf16_f32 v4, v4, v5
	v_cvt_pk_bf16_f32 v5, v6, v7
	v_pk_add_f32 v[6:7], v[98:99], 0 neg_lo:[1,1] neg_hi:[1,1]
	v_pk_add_f32 v[98:99], v[100:101], 0 neg_lo:[1,1] neg_hi:[1,1]
	v_exp_f32_e64 v194, -|v106|
	v_cvt_pk_bf16_f32 v6, v6, v7
	v_cvt_pk_bf16_f32 v7, v98, v99
	v_exp_f32_e64 v99, -|v107|
	v_add_f32_e32 v98, 1.0, v194
	v_log_f32_e32 v194, v98
	v_sub_f32_e32 v3, v3, v100
	v_add_f32_e32 v99, 1.0, v99
	v_log_f32_e32 v195, v99
	v_max_f32_e32 v100, v106, v106
	v_max_f32_e32 v98, 0, v100
	v_min_f32_e32 v106, 0, v100
	v_max_f32_e32 v100, v107, v107
	v_max_f32_e32 v99, 0, v100
	v_pk_add_f32 v[196:197], v[98:99], v[194:195]
	v_exp_f32_e64 v98, -|v108|
	v_exp_f32_e64 v99, -|v109|
	v_min_f32_e32 v107, 0, v100
	v_max_f32_e32 v100, v108, v108
	v_add_f32_e32 v98, 1.0, v98
	v_add_f32_e32 v99, 1.0, v99
	v_log_f32_e32 v198, v98
	v_log_f32_e32 v199, v99
	v_max_f32_e32 v98, 0, v100
	v_min_f32_e32 v108, 0, v100
	v_max_f32_e32 v100, v109, v109
	v_max_f32_e32 v99, 0, v100
	v_pk_add_f32 v[200:201], v[98:99], v[198:199]
	v_exp_f32_e64 v98, -|v110|
	v_exp_f32_e64 v99, -|v111|
	v_min_f32_e32 v109, 0, v100
	v_max_f32_e32 v100, v110, v110
	v_add_f32_e32 v98, 1.0, v98
	v_add_f32_e32 v99, 1.0, v99
	v_log_f32_e32 v202, v98
	v_log_f32_e32 v203, v99
	v_max_f32_e32 v98, 0, v100
	v_min_f32_e32 v110, 0, v100
	v_max_f32_e32 v100, v111, v111
	v_max_f32_e32 v99, 0, v100
	v_pk_add_f32 v[204:205], v[98:99], v[202:203]
	v_exp_f32_e64 v98, -|v112|
	v_exp_f32_e64 v99, -|v113|
	v_min_f32_e32 v111, 0, v100
	v_max_f32_e32 v100, v112, v112
	v_add_f32_e32 v98, 1.0, v98
	v_add_f32_e32 v99, 1.0, v99
	v_log_f32_e32 v206, v98
	v_log_f32_e32 v207, v99
	v_max_f32_e32 v98, 0, v100
	v_min_f32_e32 v112, 0, v100
	v_max_f32_e32 v100, v113, v113
	v_max_f32_e32 v99, 0, v100
	v_min_f32_e32 v15, 0, v15
	v_pk_add_f32 v[208:209], v[98:99], v[206:207]
	v_pk_add_f32 v[98:99], v[10:11], v[8:9] neg_lo:[0,1] neg_hi:[0,1]
	v_pk_add_f32 v[8:9], v[196:197], 0 neg_lo:[1,1] neg_hi:[1,1]
	v_pk_add_f32 v[10:11], v[200:201], 0 neg_lo:[1,1] neg_hi:[1,1]
	v_sub_f32_e32 v3, v3, v101
	v_min_f32_e32 v113, 0, v100
	v_pk_add_f32 v[100:101], v[14:15], v[12:13] neg_lo:[0,1] neg_hi:[0,1]
	v_cvt_pk_bf16_f32 v8, v8, v9
	v_cvt_pk_bf16_f32 v9, v10, v11
	v_pk_add_f32 v[10:11], v[204:205], 0 neg_lo:[1,1] neg_hi:[1,1]
	v_pk_add_f32 v[12:13], v[208:209], 0 neg_lo:[1,1] neg_hi:[1,1]
	v_pk_add_f32 v[102:103], v[102:103], v[16:17] neg_lo:[0,1] neg_hi:[0,1]
	v_exp_f32_e64 v14, -|v82|
	v_cvt_pk_bf16_f32 v10, v10, v11
	v_cvt_pk_bf16_f32 v11, v12, v13
	v_exp_f32_e64 v13, -|v83|
	v_max_f32_e32 v15, v82, v82
	v_max_f32_e32 v17, v83, v83
	v_exp_f32_e64 v82, -|v84|
	v_exp_f32_e64 v83, -|v85|
	v_sub_f32_e32 v3, v3, v196
	v_sub_f32_e32 v3, v3, v197
	v_add_f32_e32 v82, 1.0, v82
	v_add_f32_e32 v83, 1.0, v83
	v_log_f32_e32 v196, v82
	v_log_f32_e32 v197, v83
	v_max_f32_e32 v84, v84, v84
	v_max_f32_e32 v85, v85, v85
	v_min_f32_e32 v104, 0, v104
	v_min_f32_e32 v105, 0, v105
	v_max_f32_e32 v82, 0, v84
	v_max_f32_e32 v83, 0, v85
	v_pk_add_f32 v[104:105], v[104:105], v[192:193] neg_lo:[0,1] neg_hi:[0,1]
	v_pk_add_f32 v[108:109], v[108:109], v[198:199] neg_lo:[0,1] neg_hi:[0,1]
	v_exp_f32_e64 v192, -|v86|
	v_pk_add_f32 v[198:199], v[82:83], v[196:197]
	v_exp_f32_e64 v83, -|v87|
	v_sub_f32_e32 v3, v3, v200
	v_add_f32_e32 v82, 1.0, v192
	v_sub_f32_e32 v3, v3, v201
	v_add_f32_e32 v83, 1.0, v83
	v_log_f32_e32 v200, v82
	v_log_f32_e32 v201, v83
	v_max_f32_e32 v86, v86, v86
	v_max_f32_e32 v87, v87, v87
	v_max_f32_e32 v82, 0, v86
	v_max_f32_e32 v83, 0, v87
	v_pk_add_f32 v[110:111], v[110:111], v[202:203] neg_lo:[0,1] neg_hi:[0,1]
	v_exp_f32_e64 v192, -|v88|
	v_pk_add_f32 v[202:203], v[82:83], v[200:201]
	v_exp_f32_e64 v83, -|v89|
	v_add_f32_e32 v12, 1.0, v14
	v_add_f32_e32 v13, 1.0, v13
	v_sub_f32_e32 v3, v3, v204
	v_log_f32_e32 v12, v12
	v_log_f32_e32 v13, v13
	v_add_f32_e32 v82, 1.0, v192
	v_add_f32_e32 v83, 1.0, v83
	v_sub_f32_e32 v3, v3, v205
	v_log_f32_e32 v204, v82
	v_log_f32_e32 v205, v83
; #define LAS __attribute__((address_space(3)))
; __device__ __forceinline__ bf16x8 packf(const f32x16& x, int s) { u32x4 w; w.x = pk2(x[8 * s], x[8 * s + 1]); w.y = pk2(x[8 * s + 2], x[8 * s + 3]); w.z = pk2(x[8 * s + 4], x[8 * s + 5]); w.w = pk2(x[8 * s + 6], x[8 * s + 7]); return __builtin_bit_cast(bf16x8, w); }
; #define AT_MFMA(a, b, c) __builtin_amdgcn_mfma_f32_32x32x16_bf16((a), (b), (c), 0, 0, 0)
; template <bool MLA>
; __device__ __forceinline__ void attn_unit(const P& p, LAS unsigned char* lds, const int b, const int h, const int qb) {
;     ...
;                 p0 = AT_MFMA(tri0, lf[0], p0); p0 = AT_MFMA(tri1, lf[1], p0); p0 = AT_MFMA(ones, lf[2], p0); p0 = AT_MFMA(ones, lf[3], p0);
;                 p1 = AT_MFMA(tri0, lf[2], p1); p1 = AT_MFMA(tri1, lf[3], p1);
; #pragma unroll
;                 for (int r = 0; r < 16; ++r) { p0[r] = __builtin_amdgcn_exp2f(p0[r] + R2); p1[r] = __builtin_amdgcn_exp2f(p1[r] + R2); }
;                 lsum += __shfl_xor(lsum, 32);
;                 R2 += lsum;
;                 pf0 = packf(p0, 0); pf1 = packf(p0, 1); pf2 = packf(p1, 0); pf3 = packf(p1, 1);
;             }
;             const LAS unsigned char* vb = kb + KT;
; #pragma unroll
;             for (int d0 = 0; d0 < 4; ++d0) { const LAS unsigned char* vr = vb + (32 * d0 + r32) * VSTR + hi * 16;
;                 o[d0] = AT_MFMA(pf0, *(const LAS bf16x8*)(vr), o[d0]); o[d0] = AT_MFMA(pf1, *(const LAS bf16x8*)(vr + 32), o[d0]);
;                 o[d0] = AT_MFMA(pf2, *(const LAS bf16x8*)(vr + 64), o[d0]); o[d0] = AT_MFMA(pf3, *(const LAS bf16x8*)(vr + 96), o[d0]); __builtin_amdgcn_sched_barrier(0); }
	v_sub_f32_e32 v3, v3, v208
	v_max_f32_e32 v14, 0, v15
	v_min_f32_e32 v16, 0, v15
	v_max_f32_e32 v15, 0, v17
	v_max_f32_e32 v88, v88, v88
	v_max_f32_e32 v89, v89, v89
	v_sub_f32_e32 v3, v3, v209
	v_pk_add_f32 v[14:15], v[14:15], v[12:13]
	v_max_f32_e32 v82, 0, v88
	v_max_f32_e32 v83, 0, v89
	v_pk_add_f32 v[112:113], v[112:113], v[206:207] neg_lo:[0,1] neg_hi:[0,1]
	v_sub_f32_e32 v3, v3, v14
	v_pk_add_f32 v[206:207], v[82:83], v[204:205]
	v_pk_add_f32 v[82:83], v[14:15], 0 neg_lo:[1,1] neg_hi:[1,1]
	v_exp_f32_e64 v14, -|v90|
	v_cvt_pk_bf16_f32 v192, v82, v83
	v_pk_add_f32 v[82:83], v[198:199], 0 neg_lo:[1,1] neg_hi:[1,1]
	v_exp_f32_e64 v212, -|v92|
	v_add_f32_e32 v14, 1.0, v14
	v_log_f32_e32 v208, v14
	v_exp_f32_e64 v14, -|v91|
	v_cvt_pk_bf16_f32 v193, v82, v83
	v_pk_add_f32 v[82:83], v[202:203], 0 neg_lo:[1,1] neg_hi:[1,1]
	v_pk_add_f32 v[106:107], v[106:107], v[194:195] neg_lo:[0,1] neg_hi:[0,1]
	v_cvt_pk_bf16_f32 v194, v82, v83
	v_pk_add_f32 v[82:83], v[206:207], 0 neg_lo:[1,1] neg_hi:[1,1]
	v_add_f32_e32 v14, 1.0, v14
	v_cvt_pk_bf16_f32 v195, v82, v83
	v_max_f32_e32 v83, v90, v90
	v_log_f32_e32 v209, v14
	v_max_f32_e32 v14, v91, v91
	v_max_f32_e32 v82, 0, v83
	v_min_f32_e32 v90, 0, v83
	v_max_f32_e32 v83, 0, v14
	v_min_f32_e32 v91, 0, v14
	v_add_f32_e32 v14, 1.0, v212
	v_log_f32_e32 v212, v14
	v_exp_f32_e64 v14, -|v93|
	v_exp_f32_e64 v216, -|v94|
	v_pk_add_f32 v[210:211], v[82:83], v[208:209]
	v_max_f32_e32 v83, v92, v92
	v_add_f32_e32 v14, 1.0, v14
	v_log_f32_e32 v213, v14
	v_max_f32_e32 v14, v93, v93
	v_max_f32_e32 v82, 0, v83
	v_min_f32_e32 v92, 0, v83
	v_max_f32_e32 v83, 0, v14
	v_min_f32_e32 v93, 0, v14
	v_add_f32_e32 v14, 1.0, v216
	v_log_f32_e32 v216, v14
	v_exp_f32_e64 v14, -|v95|
	v_exp_f32_e64 v220, -|v96|
	v_mfma_f32_32x32x16_bf16 v[98:113], v[114:117], v[4:7], v[98:113]
	v_add_f32_e64 v214, v82, v212
	v_add_f32_e64 v215, v83, v213
	v_add_f32_e32 v14, 1.0, v14
	v_max_f32_e32 v83, v94, v94
	v_log_f32_e32 v217, v14
	v_max_f32_e32 v14, v95, v95
	v_max_f32_e32 v82, 0, v83
	v_min_f32_e32 v94, 0, v83
	v_max_f32_e32 v83, 0, v14
	v_min_f32_e32 v95, 0, v14
	v_add_f32_e32 v14, 1.0, v220
	v_log_f32_e32 v220, v14
	v_exp_f32_e64 v14, -|v97|
	v_max_f32_e32 v4, v96, v96
	v_mfma_f32_32x32x16_bf16 v[98:113], v[118:121], v[8:11], v[98:113]
	v_add_f32_e64 v218, v82, v216
	v_add_f32_e64 v219, v83, v217
	v_max_f32_e32 v82, 0, v4
	v_min_f32_e32 v96, 0, v4
	v_add_f32_e32 v4, 1.0, v14
	s_mov_b32 s85, s84
	v_log_f32_e32 v221, v4
	s_mov_b32 s86, s84
	s_mov_b32 s87, s84
	v_mov_b64_e32 v[4:5], s[84:85]
	v_mov_b64_e32 v[6:7], s[86:87]
	v_max_f32_e32 v14, v97, v97
	v_min_f32_e32 v17, 0, v17
	v_min_f32_e32 v84, 0, v84
	v_min_f32_e32 v85, 0, v85
	v_min_f32_e32 v86, 0, v86
	v_min_f32_e32 v87, 0, v87
	v_min_f32_e32 v88, 0, v88
	v_min_f32_e32 v89, 0, v89
	v_max_f32_e32 v83, 0, v14
	v_min_f32_e32 v97, 0, v14
	v_pk_add_f32 v[222:223], v[82:83], v[220:221]
	v_pk_add_f32 v[82:83], v[16:17], v[12:13] neg_lo:[0,1] neg_hi:[0,1]
	v_pk_add_f32 v[84:85], v[84:85], v[196:197] neg_lo:[0,1] neg_hi:[0,1]
	v_pk_add_f32 v[86:87], v[86:87], v[200:201] neg_lo:[0,1] neg_hi:[0,1]
	v_pk_add_f32 v[88:89], v[88:89], v[204:205] neg_lo:[0,1] neg_hi:[0,1]
	v_pk_add_f32 v[90:91], v[90:91], v[208:209] neg_lo:[0,1] neg_hi:[0,1]
	v_pk_add_f32 v[92:93], v[92:93], v[212:213] neg_lo:[0,1] neg_hi:[0,1]
	v_pk_add_f32 v[94:95], v[94:95], v[216:217] neg_lo:[0,1] neg_hi:[0,1]
	v_pk_add_f32 v[96:97], v[96:97], v[220:221] neg_lo:[0,1] neg_hi:[0,1]
	v_mfma_f32_32x32x16_bf16 v[98:113], v[4:7], v[192:195], v[98:113]
	v_add_f32_e64 v8, -v210, neg(0)
	v_add_f32_e64 v9, -v211, neg(0)
	v_add_f32_e64 v10, -v214, neg(0)
	v_add_f32_e64 v11, -v215, neg(0)
	v_cvt_pk_bf16_f32 v8, v8, v9
	v_cvt_pk_bf16_f32 v9, v10, v11
	v_pk_add_f32 v[10:11], v[218:219], 0 neg_lo:[1,1] neg_hi:[1,1]
	v_pk_add_f32 v[12:13], v[222:223], 0 neg_lo:[1,1] neg_hi:[1,1]
	v_cvt_pk_bf16_f32 v10, v10, v11
	v_mfma_f32_32x32x16_bf16 v[82:97], v[114:117], v[192:195], v[82:97]
	v_cvt_pk_bf16_f32 v11, v12, v13
	v_sub_f32_e32 v3, v3, v15
	v_sub_f32_e32 v3, v3, v198
	v_sub_f32_e32 v3, v3, v199
	v_sub_f32_e32 v3, v3, v202
	v_sub_f32_e32 v3, v3, v203
	v_sub_f32_e32 v3, v3, v206
	v_mfma_f32_32x32x16_bf16 v[82:97], v[118:121], v[8:11], v[82:97]
	v_sub_f32_e32 v3, v3, v207
	v_sub_f32_e32 v3, v3, v210
	v_sub_f32_e32 v3, v3, v211
	v_sub_f32_e32 v3, v3, v214
	v_sub_f32_e32 v3, v3, v215
	v_sub_f32_e32 v3, v3, v218
	v_sub_f32_e32 v3, v3, v219
	v_mfma_f32_32x32x16_bf16 v[98:113], v[4:7], v[8:11], v[98:113]
	s_nop 3
	v_add_f32_e32 v5, v191, v82
	v_add_f32_e32 v6, v191, v83
	v_add_f32_e32 v7, v191, v84
	v_add_f32_e32 v8, v191, v85
	v_add_f32_e32 v9, v191, v86
	v_add_f32_e32 v10, v191, v87
	v_add_f32_e32 v11, v191, v88
	s_nop 0
	v_add_f32_e32 v4, v191, v98
	v_exp_f32_e32 v16, v5
	v_add_f32_e32 v5, v191, v99
	v_exp_f32_e32 v17, v6
	v_add_f32_e32 v6, v191, v100
	v_exp_f32_e32 v98, v7
	v_add_f32_e32 v7, v191, v101
	v_exp_f32_e32 v99, v8
	v_add_f32_e32 v8, v191, v102
	v_exp_f32_e32 v86, v9
	v_add_f32_e32 v9, v191, v103
	v_exp_f32_e32 v87, v10
	v_add_f32_e32 v10, v191, v104
	v_exp_f32_e32 v88, v11
	v_add_f32_e32 v11, v191, v105
	v_add_f32_e32 v82, v191, v93
	v_exp_f32_e32 v4, v4
	v_exp_f32_e32 v5, v5
	v_exp_f32_e32 v6, v6
	v_exp_f32_e32 v7, v7
	v_exp_f32_e32 v8, v8
	v_exp_f32_e32 v9, v9
	v_exp_f32_e32 v10, v10
	v_exp_f32_e32 v11, v11
	v_exp_f32_e32 v101, v82
	v_add_f32_e32 v82, v191, v110
	v_add_f32_e32 v15, v191, v92
	v_exp_f32_e32 v92, v82
	v_add_f32_e32 v82, v191, v94
	v_exp_f32_e32 v94, v82
	v_add_f32_e32 v82, v191, v111
	v_exp_f32_e32 v93, v82
	v_add_f32_e32 v82, v191, v95
	v_add3_u32 v105, s89, v1, v186
	v_exp_f32_e32 v95, v82
	v_add_f32_e32 v82, v191, v112
	v_cvt_pk_bf16_f32 v4, v4, v5
	v_cvt_pk_bf16_f32 v5, v6, v7
	v_cvt_pk_bf16_f32 v6, v8, v9
	v_cvt_pk_bf16_f32 v7, v10, v11
	ds_read_b128 v[8:11], v105 offset:17408
	v_exp_f32_e32 v102, v82
	v_add_f32_e32 v82, v191, v96
	v_add_f32_e32 v12, v191, v89
	v_add_f32_e32 v13, v191, v90
	v_add_f32_e32 v14, v191, v91
	v_exp_f32_e32 v96, v82
	v_add_f32_e32 v82, v191, v113
	v_exp_f32_e32 v89, v12
	v_add_f32_e32 v12, v191, v106
	v_exp_f32_e32 v90, v13
	v_add_f32_e32 v13, v191, v107
	v_exp_f32_e32 v91, v14
	v_add_f32_e32 v14, v191, v108
	v_exp_f32_e32 v100, v15
	v_add_f32_e32 v15, v191, v109
	v_exp_f32_e32 v103, v82
	v_add_f32_e32 v82, v191, v97
	v_exp_f32_e32 v12, v12
	v_exp_f32_e32 v13, v13
	v_exp_f32_e32 v14, v14
	v_exp_f32_e32 v15, v15
	v_exp_f32_e32 v97, v82
	v_and_b32_e32 v82, 64, v189
	v_add_u32_e32 v106, 64, v82
	ds_read_b128 v[82:85], v105 offset:17440
	s_waitcnt lgkmcnt(1)
; #define LAS __attribute__((address_space(3)))
; __device__ __forceinline__ bf16x8 packf(const f32x16& x, int s) { u32x4 w; w.x = pk2(x[8 * s], x[8 * s + 1]); w.y = pk2(x[8 * s + 2], x[8 * s + 3]); w.z = pk2(x[8 * s + 4], x[8 * s + 5]); w.w = pk2(x[8 * s + 6], x[8 * s + 7]); return __builtin_bit_cast(bf16x8, w); }
; #define AT_MFMA(a, b, c) __builtin_amdgcn_mfma_f32_32x32x16_bf16((a), (b), (c), 0, 0, 0)
; template <bool MLA>
; __device__ __forceinline__ void attn_unit(const P& p, LAS unsigned char* lds, const int b, const int h, const int qb) {
;     ...
;                 lsum += __shfl_xor(lsum, 32);
;                 R2 += lsum;
;                 pf0 = packf(p0, 0); pf1 = packf(p0, 1); pf2 = packf(p1, 0); pf3 = packf(p1, 1);
;             }
;             const LAS unsigned char* vb = kb + KT;
; #pragma unroll
;             for (int d0 = 0; d0 < 4; ++d0) { const LAS unsigned char* vr = vb + (32 * d0 + r32) * VSTR + hi * 16;
;                 o[d0] = AT_MFMA(pf0, *(const LAS bf16x8*)(vr), o[d0]); o[d0] = AT_MFMA(pf1, *(const LAS bf16x8*)(vr + 32), o[d0]);
;                 o[d0] = AT_MFMA(pf2, *(const LAS bf16x8*)(vr + 64), o[d0]); o[d0] = AT_MFMA(pf3, *(const LAS bf16x8*)(vr + 96), o[d0]); __builtin_amdgcn_sched_barrier(0); }
	v_mfma_f32_32x32x16_bf16 v[66:81], v[4:7], v[8:11], v[66:81]
	v_cvt_pk_bf16_f32 v12, v12, v13
	v_cvt_pk_bf16_f32 v13, v14, v15
	v_cvt_pk_bf16_f32 v14, v92, v93
	v_cvt_pk_bf16_f32 v15, v102, v103
	v_cvt_pk_bf16_f32 v8, v16, v17
	v_cvt_pk_bf16_f32 v9, v98, v99
	v_cvt_pk_bf16_f32 v10, v86, v87
	s_waitcnt lgkmcnt(0)
	v_mfma_f32_32x32x16_bf16 v[66:81], v[12:15], v[82:85], v[66:81]
	v_cvt_pk_bf16_f32 v11, v88, v89
	ds_read_b128 v[82:85], v105 offset:17472
	v_xor_b32_e32 v104, 32, v189
	v_cmp_lt_i32_e32 vcc, v104, v106
	v_cvt_pk_bf16_f32 v86, v90, v91
	v_cvt_pk_bf16_f32 v87, v100, v101
	v_cndmask_b32_e32 v92, v189, v104, vcc
	v_lshlrev_b32_e32 v16, 2, v92
	ds_read_b128 v[90:93], v105 offset:17504
	s_waitcnt lgkmcnt(1)
	v_mfma_f32_32x32x16_bf16 v[66:81], v[8:11], v[82:85], v[66:81]
	v_cvt_pk_bf16_f32 v88, v94, v95
	v_cvt_pk_bf16_f32 v89, v96, v97
	v_sub_f32_e32 v3, v3, v222
	v_sub_f32_e32 v3, v3, v223
	v_mov_b32_e32 v16, v3
	s_nop 1
	v_permlane32_swap_b32 v3, v16
	s_waitcnt lgkmcnt(0)
	v_add_f32_e32 v3, v3, v16
	v_mfma_f32_32x32x16_bf16 v[66:81], v[86:89], v[90:93], v[66:81]
	ds_read_b128 v[82:85], v105 offset:22016
	ds_read_b128 v[90:93], v105 offset:22048
	s_waitcnt lgkmcnt(1)
	v_mfma_f32_32x32x16_bf16 v[34:49], v[4:7], v[82:85], v[34:49]
	s_waitcnt lgkmcnt(0)
	v_mfma_f32_32x32x16_bf16 v[34:49], v[12:15], v[90:93], v[34:49]
	ds_read_b128 v[82:85], v105 offset:22080
	ds_read_b128 v[90:93], v105 offset:22112
	s_waitcnt lgkmcnt(1)
	v_mfma_f32_32x32x16_bf16 v[34:49], v[8:11], v[82:85], v[34:49]
	s_waitcnt lgkmcnt(0)
	v_mfma_f32_32x32x16_bf16 v[34:49], v[86:89], v[90:93], v[34:49]
	ds_read_b128 v[82:85], v105 offset:26624
	ds_read_b128 v[90:93], v105 offset:26656
	s_waitcnt lgkmcnt(1)
	v_mfma_f32_32x32x16_bf16 v[18:33], v[4:7], v[82:85], v[18:33]
	s_waitcnt lgkmcnt(0)
	v_mfma_f32_32x32x16_bf16 v[18:33], v[12:15], v[90:93], v[18:33]
	ds_read_b128 v[82:85], v105 offset:26688
	ds_read_b128 v[90:93], v105 offset:26720
	s_waitcnt lgkmcnt(1)
	v_mfma_f32_32x32x16_bf16 v[18:33], v[8:11], v[82:85], v[18:33]
	s_waitcnt lgkmcnt(0)
	v_mfma_f32_32x32x16_bf16 v[18:33], v[86:89], v[90:93], v[18:33]
	ds_read_b128 v[82:85], v105 offset:31232
	ds_read_b128 v[90:93], v105 offset:31264
	s_waitcnt lgkmcnt(1)
	v_mfma_f32_32x32x16_bf16 v[50:65], v[4:7], v[82:85], v[50:65]
	s_waitcnt lgkmcnt(0)
	v_mfma_f32_32x32x16_bf16 v[50:65], v[12:15], v[90:93], v[50:65]
	ds_read_b128 v[4:7], v105 offset:31296
	ds_read_b128 v[12:15], v105 offset:31328
	s_waitcnt lgkmcnt(1)
	v_mfma_f32_32x32x16_bf16 v[50:65], v[8:11], v[4:7], v[50:65]
	s_waitcnt lgkmcnt(0)
	v_mfma_f32_32x32x16_bf16 v[50:65], v[86:89], v[12:15], v[50:65]
	v_add_f32_e32 v191, v191, v3

; template <bool MLA>
; __device__ __forceinline__ void attn_unit(const P& p, LAS unsigned char* lds, const int b, const int h, const int qb) {
;     ...
;                 for (int r = 0; r < 16; ++r) pm = fmaxf(pm, fmaxf(p0[r], p1[r]));
;                 pm = fmaxf(pm, __shfl_xor(pm, 32));
;                 const float mn = fmaxf(m_run, pm), alpha = __builtin_amdgcn_exp2f(m_run - mn); m_run = mn;
;                 float ps = 0.f;
; #pragma unroll
;                 for (int r = 0; r < 16; ++r) { p0[r] = __builtin_amdgcn_exp2f(p0[r] - mn); p1[r] = __builtin_amdgcn_exp2f(p1[r] - mn); ps += p0[r] + p1[r]; }
;                 ps += __shfl_xor(ps, 32);
;                 l_run = l_run * alpha + ps;
;                 if (__any(alpha < 1.f)) { if (hi == 0) al[r32] = alpha; asm volatile("s_waitcnt lgkmcnt(0)" ::: "memory");
; #pragma unroll
;                     for (int r = 0; r < 16; ++r) { const float a = al[(r & 3) + 8 * (r >> 2) + 4 * hi];
; #pragma unroll
;                         for (int d0 = 0; d0 < 4; ++d0) o[d0][r] *= a; } }
.LBB0_877:
	s_nop 8
	s_mov_b32 s0, 0xff61b1e6
	v_max3_f32 v3, v82, v83, s0
	v_max3_f32 v4, v84, v85, v86
	v_max3_f32 v5, v87, v88, v89
	v_max3_f32 v3, v3, v90, v91
	v_max3_f32 v4, v4, v92, v93
	v_max3_f32 v5, v5, v94, v95
	v_max3_f32 v3, v3, v96, v97
	v_max3_f32 v4, v4, v98, v99
	v_max3_f32 v5, v5, v100, v101
	v_max3_f32 v3, v3, v102, v103
	v_max3_f32 v4, v4, v104, v105
	v_max3_f32 v5, v5, v106, v107
	v_max3_f32 v3, v3, v108, v109
	v_max3_f32 v4, v4, v110, v111
	v_max3_f32 v5, v5, v112, v113
	v_max3_f32 v3, v3, v4, v5
	v_mov_b32_e32 v4, v3
	s_nop 1
	v_permlane32_swap_b32 v3, v4
	v_max_f32_e32 v3, v3, v4
	v_add_f32_e32 v4, 0xc1000000, v3
	v_cmp_gt_f32_e32 vcc, v4, v219
	s_nop 1
	v_cndmask_b32_e32 v3, v219, v3, vcc
	v_sub_f32_e32 v4, v82, v3
	v_exp_f32_e32 v10, v4
	v_sub_f32_e32 v4, v98, v3
	v_exp_f32_e32 v4, v4
	v_sub_f32_e32 v5, v83, v3
	v_exp_f32_e32 v12, v5
	v_sub_f32_e32 v5, v99, v3
	v_add_f32_e32 v6, v10, v4
	v_add_f32_e32 v8, 0, v6
	v_sub_f32_e32 v6, v84, v3
	v_exp_f32_e32 v5, v5
	v_exp_f32_e32 v14, v6
	v_sub_f32_e32 v6, v100, v3
	v_exp_f32_e32 v6, v6
	v_add_f32_e32 v9, v12, v5
	v_sub_f32_e32 v7, v85, v3
	v_add_f32_e32 v8, v9, v8
	v_add_f32_e32 v9, v14, v6
	v_exp_f32_e32 v16, v7
	v_sub_f32_e32 v7, v101, v3
	v_add_f32_e32 v11, v9, v8
	v_sub_f32_e32 v8, v86, v3
	v_exp_f32_e32 v7, v7
	v_exp_f32_e32 v84, v8
	v_sub_f32_e32 v8, v102, v3
	v_exp_f32_e32 v8, v8
	v_add_f32_e32 v13, v16, v7
	v_sub_f32_e32 v9, v87, v3
	v_add_f32_e32 v11, v13, v11
	v_add_f32_e32 v13, v84, v8
	v_exp_f32_e32 v87, v9
	v_sub_f32_e32 v9, v103, v3
	v_add_f32_e32 v15, v13, v11
	v_sub_f32_e32 v11, v88, v3
	v_exp_f32_e32 v9, v9
	v_exp_f32_e32 v98, v11
	v_sub_f32_e32 v11, v104, v3
	v_exp_f32_e32 v11, v11
	v_add_f32_e32 v17, v87, v9
	v_sub_f32_e32 v13, v89, v3
	v_add_f32_e32 v15, v17, v15
	v_add_f32_e32 v17, v98, v11
	v_exp_f32_e32 v99, v13
	v_sub_f32_e32 v13, v105, v3
	v_add_f32_e32 v82, v17, v15
	v_sub_f32_e32 v15, v90, v3
	v_exp_f32_e32 v13, v13
	v_exp_f32_e32 v83, v15
	v_sub_f32_e32 v15, v106, v3
	v_exp_f32_e32 v15, v15
	v_add_f32_e32 v85, v99, v13
	v_sub_f32_e32 v17, v91, v3
	v_add_f32_e32 v82, v85, v82
	v_add_f32_e32 v85, v83, v15
	v_exp_f32_e32 v86, v17
	v_sub_f32_e32 v17, v107, v3
	v_add_f32_e32 v89, v85, v82
	v_sub_f32_e32 v82, v92, v3
	v_exp_f32_e32 v17, v17
	v_exp_f32_e32 v88, v82
	v_sub_f32_e32 v82, v108, v3
	v_exp_f32_e32 v82, v82
	v_add_f32_e32 v91, v86, v17
	v_sub_f32_e32 v85, v93, v3
	v_add_f32_e32 v89, v91, v89
	v_add_f32_e32 v91, v88, v82
	v_exp_f32_e32 v90, v85
	v_sub_f32_e32 v85, v109, v3
	v_add_f32_e32 v93, v91, v89
	v_sub_f32_e32 v89, v94, v3
	v_exp_f32_e32 v85, v85
	v_exp_f32_e32 v92, v89
	v_sub_f32_e32 v89, v110, v3
	v_exp_f32_e32 v89, v89
	v_add_f32_e32 v100, v90, v85
	v_sub_f32_e32 v91, v95, v3
	v_add_f32_e32 v93, v100, v93
	v_add_f32_e32 v95, v92, v89
	v_exp_f32_e32 v94, v91
	v_sub_f32_e32 v91, v111, v3
	v_add_f32_e32 v100, v95, v93
	v_sub_f32_e32 v93, v96, v3
	v_exp_f32_e32 v91, v91
	v_exp_f32_e32 v101, v93
	v_sub_f32_e32 v93, v112, v3
	v_sub_f32_e32 v95, v97, v3
	v_exp_f32_e32 v93, v93
	v_exp_f32_e32 v102, v95
	v_sub_f32_e32 v95, v113, v3
	v_exp_f32_e32 v95, v95
	v_add_f32_e32 v103, v94, v91
	v_add_f32_e32 v96, v103, v100
	v_add_f32_e32 v97, v101, v93
	v_add_f32_e32 v97, v97, v96
	v_add_f32_e32 v100, v102, v95
	v_sub_f32_e32 v219, v219, v3
	v_add_f32_e32 v97, v100, v97
	v_exp_f32_e32 v96, v219
	v_mov_b32_e32 v100, v97
	s_nop 1
	v_permlane32_swap_b32 v97, v100
	v_cmp_gt_f32_e32 vcc, 1.0, v96
	s_cbranch_vccz .LBB0_881
	s_and_saveexec_b64 s[0:1], s[4:5]
	ds_write_b32 v215, v96
	s_or_b64 exec, exec, s[0:1]
	s_waitcnt lgkmcnt(0)
	ds_read_b128 v[104:107], v217 offset:96
	ds_read_b128 v[108:111], v217 offset:64
	ds_read_b128 v[220:223], v217 offset:32
	ds_read_b128 v[224:227], v217
	s_waitcnt lgkmcnt(3)
	v_pk_mul_f32 v[80:81], v[80:81], v[106:107]
	s_waitcnt lgkmcnt(2)
	v_pk_mul_f32 v[76:77], v[76:77], v[110:111]
	s_waitcnt lgkmcnt(1)
	v_pk_mul_f32 v[72:73], v[72:73], v[222:223]
	s_waitcnt lgkmcnt(0)
	v_pk_mul_f32 v[68:69], v[68:69], v[226:227]
	v_pk_mul_f32 v[78:79], v[78:79], v[104:105]
	v_pk_mul_f32 v[74:75], v[74:75], v[108:109]
	v_pk_mul_f32 v[70:71], v[70:71], v[220:221]
	v_pk_mul_f32 v[66:67], v[66:67], v[224:225]
	v_pk_mul_f32 v[64:65], v[64:65], v[106:107]
	v_pk_mul_f32 v[60:61], v[60:61], v[110:111]
	v_pk_mul_f32 v[56:57], v[56:57], v[222:223]
	v_pk_mul_f32 v[52:53], v[52:53], v[226:227]
	v_pk_mul_f32 v[62:63], v[62:63], v[104:105]
	v_pk_mul_f32 v[58:59], v[58:59], v[108:109]
	v_pk_mul_f32 v[54:55], v[54:55], v[220:221]
	v_pk_mul_f32 v[50:51], v[50:51], v[224:225]
	v_pk_mul_f32 v[48:49], v[48:49], v[106:107]
	v_pk_mul_f32 v[44:45], v[44:45], v[110:111]
	v_pk_mul_f32 v[40:41], v[40:41], v[222:223]
	v_pk_mul_f32 v[36:37], v[36:37], v[226:227]
	v_pk_mul_f32 v[46:47], v[46:47], v[104:105]
	v_pk_mul_f32 v[42:43], v[42:43], v[108:109]
	v_pk_mul_f32 v[38:39], v[38:39], v[220:221]
	v_pk_mul_f32 v[34:35], v[34:35], v[224:225]
	v_pk_mul_f32 v[32:33], v[32:33], v[106:107]
	v_pk_mul_f32 v[28:29], v[28:29], v[110:111]
	v_pk_mul_f32 v[24:25], v[24:25], v[222:223]
	v_pk_mul_f32 v[20:21], v[20:21], v[226:227]
	v_pk_mul_f32 v[30:31], v[30:31], v[104:105]
	v_pk_mul_f32 v[26:27], v[26:27], v[108:109]
	v_pk_mul_f32 v[22:23], v[22:23], v[220:221]
	v_pk_mul_f32 v[18:19], v[18:19], v[224:225]
